# v94 + nt on the phase-4 epilogue loads of the f32 input x (134 MB read exactly once while the out-projection GEMM streams its operands)
# baseline (speedup 1.0000x reference)
.LBB0_425:
	s_andn2_saveexec_b64 s[22:23], s[22:23]
	v_max_i32_e32 v136, 0x70, v158
	v_add_u32_e32 v136, 0xffffff90, v136
	s_or_b64 exec, exec, s[22:23]
	v_lshl_or_b32 v146, s18, 8, v154
	v_lshlrev_b64 v[160:161], 13, v[136:137]
	v_ashrrev_i32_e32 v147, 31, v146
	v_lshl_add_u64 v[150:151], v[150:151], 0, v[160:161]
	v_lshl_add_u64 v[150:151], v[146:147], 2, v[150:151]
	global_load_dwordx4 v[160:163], v[150:151], off nt
	global_load_dwordx4 v[164:167], v[150:151], off offset:16 nt
	v_ashrrev_i32_e32 v149, 31, v148
	v_cmp_gt_i32_e32 vcc, s46, v158
	v_lshlrev_b64 v[158:159], 12, v[148:149]
	v_lshl_add_u64 v[158:159], s[96:97], 0, v[158:159]
	v_cndmask_b32_e64 v136, 1.0, 0, vcc
	v_lshl_add_u64 v[168:169], v[146:147], 1, v[158:159]
	v_readlane_b32 s76, v250, 7
	v_readlane_b32 s78, v250, 9
	v_readlane_b32 s79, v250, 10
	v_readlane_b32 s77, v250, 8
	v_readlane_b32 s80, v250, 11
	v_readlane_b32 s81, v250, 12
	v_readlane_b32 s82, v250, 13
	v_readlane_b32 s83, v250, 14
	v_readlane_b32 s84, v250, 15
	v_readlane_b32 s85, v250, 16
	v_readlane_b32 s86, v250, 17
	v_readlane_b32 s87, v250, 18
	v_readlane_b32 s88, v250, 19
	v_readlane_b32 s89, v250, 20
	v_readlane_b32 s90, v250, 21
	v_readlane_b32 s91, v250, 22
	s_waitcnt vmcnt(0)
	v_fma_f32 v124, v136, v160, v124
	v_fmac_f32_e32 v123, v136, v167
	v_fma_f32 v125, v136, v161, v125
	v_fma_f32 v126, v136, v162, v126
	v_fmac_f32_e32 v127, v136, v163
	v_fma_f32 v149, v136, v164, v120
	v_fma_f32 v158, v136, v165, v121
	v_fma_f32 v159, v136, v166, v122
	v_cvt_pk_bf16_f32 v120, v124, v125
	v_cvt_pk_bf16_f32 v121, v126, v127
	v_cvt_pk_bf16_f32 v122, v149, v158
	v_cvt_pk_bf16_f32 v123, v159, v123
	global_store_dwordx4 v[168:169], v[120:123], off
	global_load_dwordx4 v[158:161], v[150:151], off offset:512 nt
	global_load_dwordx4 v[162:165], v[150:151], off offset:528 nt
	v_or_b32_e32 v120, 16, v148
	v_mul_hi_i32 v121, v120, s43
	v_lshrrev_b32_e32 v122, 31, v121
	v_ashrrev_i32_e32 v121, 10, v121
	v_add_u32_e32 v122, v121, v122
	v_mad_i32_i24 v124, v122, s44, v120
	v_cmp_lt_i32_e32 vcc, s45, v124
	s_waitcnt vmcnt(1)
	v_fma_f32 v116, v136, v158, v116
	v_fma_f32 v117, v136, v159, v117
	v_fma_f32 v118, v136, v160, v118
	v_fmac_f32_e32 v119, v136, v161
	s_waitcnt vmcnt(0)
	v_fma_f32 v121, v136, v162, v112
	v_fma_f32 v123, v136, v163, v113
	v_fmac_f32_e32 v115, v136, v165
	v_cvt_pk_bf16_f32 v112, v116, v117
	v_cvt_pk_bf16_f32 v113, v118, v119
	v_fma_f32 v125, v136, v164, v114
	v_cvt_pk_bf16_f32 v114, v121, v123
	v_cvt_pk_bf16_f32 v115, v125, v115
	global_store_dwordx4 v[168:169], v[112:115], off offset:256
	s_nop 1
	v_mov_b64_e32 v[112:113], s[78:79]
	s_and_saveexec_b64 s[18:19], vcc
	s_xor_b64 s[18:19], exec, s[18:19]
	s_mov_b32 s60, s66
	v_readlane_b32 s59, v250, 50
	s_cbranch_execz .LBB0_429
	v_ashrrev_i32_e32 v123, 31, v122
	v_readlane_b32 s76, v250, 7
	v_lshlrev_b64 v[112:113], 25, v[122:123]
	v_readlane_b32 s77, v250, 8
	v_add_u32_e32 v136, 0xffffff80, v124
	v_readlane_b32 s78, v250, 9
	v_lshl_add_u64 v[112:113], s[76:77], 0, v[112:113]
	v_readlane_b32 s79, v250, 10
	v_readlane_b32 s80, v250, 11
	v_readlane_b32 s81, v250, 12
	v_readlane_b32 s82, v250, 13
	v_readlane_b32 s83, v250, 14
	v_readlane_b32 s84, v250, 15
	v_readlane_b32 s85, v250, 16
	v_readlane_b32 s86, v250, 17
	v_readlane_b32 s87, v250, 18
	v_readlane_b32 s88, v250, 19
	v_readlane_b32 s89, v250, 20
	v_readlane_b32 s90, v250, 21
	v_readlane_b32 s91, v250, 22
.LBB0_429:
	s_andn2_saveexec_b64 s[18:19], s[18:19]
	v_max_i32_e32 v114, 0x70, v124
	v_add_u32_e32 v136, 0xffffff90, v114
	s_or_b64 exec, exec, s[18:19]
	v_lshlrev_b64 v[114:115], 13, v[136:137]
	v_lshl_add_u64 v[112:113], v[112:113], 0, v[114:115]
	v_lshl_add_u64 v[122:123], v[146:147], 2, v[112:113]
	global_load_dwordx4 v[112:115], v[122:123], off nt
	global_load_dwordx4 v[116:119], v[122:123], off offset:16 nt
	v_ashrrev_i32_e32 v121, 31, v120
	v_cmp_gt_i32_e32 vcc, s46, v124
	v_lshlrev_b64 v[120:121], 12, v[120:121]
	v_lshl_add_u64 v[120:121], s[96:97], 0, v[120:121]
	v_cndmask_b32_e64 v124, 1.0, 0, vcc
	v_lshl_add_u64 v[120:121], v[146:147], 1, v[120:121]
	v_readlane_b32 s76, v250, 7
	v_readlane_b32 s78, v250, 9
	v_readlane_b32 s79, v250, 10
	v_readlane_b32 s77, v250, 8
	v_readlane_b32 s80, v250, 11
	v_readlane_b32 s81, v250, 12
	v_readlane_b32 s82, v250, 13
	v_readlane_b32 s83, v250, 14
	v_readlane_b32 s84, v250, 15
	v_readlane_b32 s85, v250, 16
	v_readlane_b32 s86, v250, 17
	v_readlane_b32 s87, v250, 18
	v_readlane_b32 s88, v250, 19
	v_readlane_b32 s89, v250, 20
	v_readlane_b32 s90, v250, 21
	v_readlane_b32 s91, v250, 22
	s_waitcnt vmcnt(1)
	v_fma_f32 v108, v124, v112, v108
	s_waitcnt vmcnt(0)
	v_fmac_f32_e32 v107, v124, v119
	v_fma_f32 v109, v124, v113, v109
	v_fma_f32 v110, v124, v114, v110
	v_fmac_f32_e32 v111, v124, v115
	v_fma_f32 v112, v124, v116, v104
	v_fma_f32 v113, v124, v117, v105
	v_fma_f32 v114, v124, v118, v106
	v_cvt_pk_bf16_f32 v104, v108, v109
	v_cvt_pk_bf16_f32 v105, v110, v111
	v_cvt_pk_bf16_f32 v106, v112, v113
	v_cvt_pk_bf16_f32 v107, v114, v107
	global_store_dwordx4 v[120:121], v[104:107], off
	global_load_dwordx4 v[110:113], v[122:123], off offset:512 nt
	global_load_dwordx4 v[114:117], v[122:123], off offset:528 nt
	v_or_b32_e32 v104, 32, v148
	v_mul_hi_i32 v105, v104, s43
	v_lshrrev_b32_e32 v106, 31, v105
	v_ashrrev_i32_e32 v105, 10, v105
	v_add_u32_e32 v106, v105, v106
	v_mad_i32_i24 v108, v106, s44, v104
	v_cmp_lt_i32_e32 vcc, s45, v108
	s_waitcnt vmcnt(1)
	v_fma_f32 v100, v124, v110, v100
	v_fma_f32 v101, v124, v111, v101
	v_fma_f32 v102, v124, v112, v102
	v_fmac_f32_e32 v103, v124, v113
	s_waitcnt vmcnt(0)
	v_fma_f32 v105, v124, v114, v96
	v_fma_f32 v107, v124, v115, v97
	v_fmac_f32_e32 v99, v124, v117
	v_cvt_pk_bf16_f32 v96, v100, v101
	v_cvt_pk_bf16_f32 v97, v102, v103
	v_fma_f32 v109, v124, v116, v98
	v_cvt_pk_bf16_f32 v98, v105, v107
	v_cvt_pk_bf16_f32 v99, v109, v99
	global_store_dwordx4 v[120:121], v[96:99], off offset:256
	s_nop 1
	v_mov_b64_e32 v[96:97], s[78:79]
	s_and_saveexec_b64 s[18:19], vcc
	s_xor_b64 s[18:19], exec, s[18:19]
	s_cbranch_execz .LBB0_433
	v_ashrrev_i32_e32 v107, 31, v106
	v_readlane_b32 s76, v250, 7
	v_lshlrev_b64 v[96:97], 25, v[106:107]
	v_readlane_b32 s77, v250, 8
	v_add_u32_e32 v136, 0xffffff80, v108
	v_readlane_b32 s78, v250, 9
	v_lshl_add_u64 v[96:97], s[76:77], 0, v[96:97]
	v_readlane_b32 s79, v250, 10
	v_readlane_b32 s80, v250, 11
	v_readlane_b32 s81, v250, 12
	v_readlane_b32 s82, v250, 13
	v_readlane_b32 s83, v250, 14
	v_readlane_b32 s84, v250, 15
	v_readlane_b32 s85, v250, 16
	v_readlane_b32 s86, v250, 17
	v_readlane_b32 s87, v250, 18
	v_readlane_b32 s88, v250, 19
	v_readlane_b32 s89, v250, 20
	v_readlane_b32 s90, v250, 21
	v_readlane_b32 s91, v250, 22
.LBB0_433:
	s_andn2_saveexec_b64 s[18:19], s[18:19]
	v_max_i32_e32 v98, 0x70, v108
	v_add_u32_e32 v136, 0xffffff90, v98
	s_or_b64 exec, exec, s[18:19]
	v_lshlrev_b64 v[98:99], 13, v[136:137]
	v_lshl_add_u64 v[96:97], v[96:97], 0, v[98:99]
	v_lshl_add_u64 v[106:107], v[146:147], 2, v[96:97]
	global_load_dwordx4 v[96:99], v[106:107], off nt
	global_load_dwordx4 v[100:103], v[106:107], off offset:16 nt
	v_ashrrev_i32_e32 v105, 31, v104
	v_cmp_gt_i32_e32 vcc, s46, v108
	v_lshlrev_b64 v[104:105], 12, v[104:105]
	v_lshl_add_u64 v[104:105], s[96:97], 0, v[104:105]
	v_cndmask_b32_e64 v108, 1.0, 0, vcc
	v_lshl_add_u64 v[104:105], v[146:147], 1, v[104:105]
	v_readlane_b32 s76, v250, 7
	v_readlane_b32 s78, v250, 9
	v_readlane_b32 s79, v250, 10
	v_readlane_b32 s77, v250, 8
	v_readlane_b32 s80, v250, 11
	v_readlane_b32 s81, v250, 12
	v_readlane_b32 s82, v250, 13
	v_readlane_b32 s83, v250, 14
	v_readlane_b32 s84, v250, 15
	v_readlane_b32 s85, v250, 16
	v_readlane_b32 s86, v250, 17
	v_readlane_b32 s87, v250, 18
	v_readlane_b32 s88, v250, 19
	v_readlane_b32 s89, v250, 20
	v_readlane_b32 s90, v250, 21
	v_readlane_b32 s91, v250, 22
	s_waitcnt vmcnt(1)
	v_fma_f32 v92, v108, v96, v92
	s_waitcnt vmcnt(0)
	v_fmac_f32_e32 v91, v108, v103
	v_fma_f32 v93, v108, v97, v93
	v_fma_f32 v94, v108, v98, v94
	v_fmac_f32_e32 v95, v108, v99
	v_fma_f32 v96, v108, v100, v88
	v_fma_f32 v97, v108, v101, v89
	v_fma_f32 v98, v108, v102, v90
	v_cvt_pk_bf16_f32 v88, v92, v93
	v_cvt_pk_bf16_f32 v89, v94, v95
	v_cvt_pk_bf16_f32 v90, v96, v97
	v_cvt_pk_bf16_f32 v91, v98, v91
	global_store_dwordx4 v[104:105], v[88:91], off
	global_load_dwordx4 v[94:97], v[106:107], off offset:512 nt
	global_load_dwordx4 v[98:101], v[106:107], off offset:528 nt
	v_or_b32_e32 v88, 48, v148
	v_mul_hi_i32 v89, v88, s43
	v_lshrrev_b32_e32 v90, 31, v89
	v_ashrrev_i32_e32 v89, 10, v89
	v_add_u32_e32 v90, v89, v90
	v_mad_i32_i24 v92, v90, s44, v88
	v_cmp_lt_i32_e32 vcc, s45, v92
	s_waitcnt vmcnt(1)
	v_fma_f32 v84, v108, v94, v84
	v_fma_f32 v85, v108, v95, v85
	v_fma_f32 v86, v108, v96, v86
	v_fmac_f32_e32 v87, v108, v97
	s_waitcnt vmcnt(0)
	v_fma_f32 v89, v108, v98, v80
	v_fma_f32 v91, v108, v99, v81
	v_fmac_f32_e32 v83, v108, v101
	v_cvt_pk_bf16_f32 v80, v84, v85
	v_cvt_pk_bf16_f32 v81, v86, v87
	v_fma_f32 v93, v108, v100, v82
	v_cvt_pk_bf16_f32 v82, v89, v91
	v_cvt_pk_bf16_f32 v83, v93, v83
	global_store_dwordx4 v[104:105], v[80:83], off offset:256
	s_nop 1
	v_mov_b64_e32 v[80:81], s[78:79]
	s_and_saveexec_b64 s[18:19], vcc
	s_xor_b64 s[18:19], exec, s[18:19]
	s_cbranch_execz .LBB0_437
	v_ashrrev_i32_e32 v91, 31, v90
	v_readlane_b32 s76, v250, 7
	v_lshlrev_b64 v[80:81], 25, v[90:91]
	v_readlane_b32 s77, v250, 8
	v_add_u32_e32 v136, 0xffffff80, v92
	v_readlane_b32 s78, v250, 9
	v_lshl_add_u64 v[80:81], s[76:77], 0, v[80:81]
	v_readlane_b32 s79, v250, 10
	v_readlane_b32 s80, v250, 11
	v_readlane_b32 s81, v250, 12
	v_readlane_b32 s82, v250, 13
	v_readlane_b32 s83, v250, 14
	v_readlane_b32 s84, v250, 15
	v_readlane_b32 s85, v250, 16
	v_readlane_b32 s86, v250, 17
	v_readlane_b32 s87, v250, 18
	v_readlane_b32 s88, v250, 19
	v_readlane_b32 s89, v250, 20
	v_readlane_b32 s90, v250, 21
	v_readlane_b32 s91, v250, 22
.LBB0_437:
	s_andn2_saveexec_b64 s[18:19], s[18:19]
	v_max_i32_e32 v82, 0x70, v92
	v_add_u32_e32 v136, 0xffffff90, v82
	s_or_b64 exec, exec, s[18:19]
	v_lshlrev_b64 v[82:83], 13, v[136:137]
	v_lshl_add_u64 v[80:81], v[80:81], 0, v[82:83]
	v_lshl_add_u64 v[90:91], v[146:147], 2, v[80:81]
	global_load_dwordx4 v[80:83], v[90:91], off nt
	global_load_dwordx4 v[84:87], v[90:91], off offset:16 nt
	v_ashrrev_i32_e32 v89, 31, v88
	v_cmp_gt_i32_e32 vcc, s46, v92
	v_lshlrev_b64 v[88:89], 12, v[88:89]
	v_lshl_add_u64 v[88:89], s[96:97], 0, v[88:89]
	v_cndmask_b32_e64 v92, 1.0, 0, vcc
	v_lshl_add_u64 v[88:89], v[146:147], 1, v[88:89]
	v_readlane_b32 s76, v250, 7
	v_readlane_b32 s78, v250, 9
	v_readlane_b32 s79, v250, 10
	v_readlane_b32 s77, v250, 8
	v_readlane_b32 s80, v250, 11
	v_readlane_b32 s81, v250, 12
	v_readlane_b32 s82, v250, 13
	v_readlane_b32 s83, v250, 14
	v_readlane_b32 s84, v250, 15
	v_readlane_b32 s85, v250, 16
	v_readlane_b32 s86, v250, 17
	v_readlane_b32 s87, v250, 18
	v_readlane_b32 s88, v250, 19
	v_readlane_b32 s89, v250, 20
	v_readlane_b32 s90, v250, 21
	v_readlane_b32 s91, v250, 22
	s_waitcnt vmcnt(1)
	v_fma_f32 v76, v92, v80, v76
	s_waitcnt vmcnt(0)
	v_fmac_f32_e32 v75, v92, v87
	v_fma_f32 v77, v92, v81, v77
	v_fma_f32 v78, v92, v82, v78
	v_fmac_f32_e32 v79, v92, v83
	v_fma_f32 v80, v92, v84, v72
	v_fma_f32 v81, v92, v85, v73
	v_fma_f32 v82, v92, v86, v74
	v_cvt_pk_bf16_f32 v72, v76, v77
	v_cvt_pk_bf16_f32 v73, v78, v79
	v_cvt_pk_bf16_f32 v74, v80, v81
	v_cvt_pk_bf16_f32 v75, v82, v75
	global_store_dwordx4 v[88:89], v[72:75], off
	global_load_dwordx4 v[78:81], v[90:91], off offset:512 nt
	global_load_dwordx4 v[82:85], v[90:91], off offset:528 nt
	v_add_u32_e32 v72, 0x80, v148
	v_mul_hi_i32 v73, v72, s43
	v_lshrrev_b32_e32 v74, 31, v73
	v_ashrrev_i32_e32 v73, 10, v73
	v_add_u32_e32 v74, v73, v74
	v_mad_i32_i24 v76, v74, s44, v72
	v_cmp_lt_i32_e32 vcc, s45, v76
	s_waitcnt vmcnt(1)
	v_fma_f32 v68, v92, v78, v68
	v_fma_f32 v69, v92, v79, v69
	v_fma_f32 v70, v92, v80, v70
	v_fmac_f32_e32 v71, v92, v81
	s_waitcnt vmcnt(0)
	v_fma_f32 v73, v92, v82, v64
	v_fma_f32 v75, v92, v83, v65
	v_fmac_f32_e32 v67, v92, v85
	v_cvt_pk_bf16_f32 v64, v68, v69
	v_cvt_pk_bf16_f32 v65, v70, v71
	v_fma_f32 v77, v92, v84, v66
	v_cvt_pk_bf16_f32 v66, v73, v75
	v_cvt_pk_bf16_f32 v67, v77, v67
	global_store_dwordx4 v[88:89], v[64:67], off offset:256
	s_nop 1
	v_mov_b64_e32 v[64:65], s[78:79]
	s_and_saveexec_b64 s[18:19], vcc
	s_xor_b64 s[18:19], exec, s[18:19]
	s_cbranch_execz .LBB0_441
	v_mul_i32_i24_e32 v64, 0xffffef80, v74
	v_ashrrev_i32_e32 v75, 31, v74
	v_readlane_b32 s76, v250, 7
	v_add_u32_e32 v136, v64, v148
	v_lshlrev_b64 v[64:65], 25, v[74:75]
	v_readlane_b32 s77, v250, 8
	v_readlane_b32 s78, v250, 9
	v_readlane_b32 s79, v250, 10
	v_lshl_add_u64 v[64:65], s[76:77], 0, v[64:65]
	v_readlane_b32 s80, v250, 11
	v_readlane_b32 s81, v250, 12
	v_readlane_b32 s82, v250, 13
	v_readlane_b32 s83, v250, 14
	v_readlane_b32 s84, v250, 15
	v_readlane_b32 s85, v250, 16
	v_readlane_b32 s86, v250, 17
	v_readlane_b32 s87, v250, 18
	v_readlane_b32 s88, v250, 19
	v_readlane_b32 s89, v250, 20
	v_readlane_b32 s90, v250, 21
	v_readlane_b32 s91, v250, 22
.LBB0_441:
	s_andn2_saveexec_b64 s[18:19], s[18:19]
	v_max_i32_e32 v66, 0x70, v76
	v_add_u32_e32 v136, 0xffffff90, v66
	s_or_b64 exec, exec, s[18:19]
	v_lshlrev_b64 v[66:67], 13, v[136:137]
	v_lshl_add_u64 v[64:65], v[64:65], 0, v[66:67]
	v_lshl_add_u64 v[74:75], v[146:147], 2, v[64:65]
	global_load_dwordx4 v[64:67], v[74:75], off nt
	global_load_dwordx4 v[68:71], v[74:75], off offset:16 nt
	v_ashrrev_i32_e32 v73, 31, v72
	v_cmp_gt_i32_e32 vcc, s46, v76
	v_lshlrev_b64 v[72:73], 12, v[72:73]
	v_lshl_add_u64 v[72:73], s[96:97], 0, v[72:73]
	v_cndmask_b32_e64 v76, 1.0, 0, vcc
	v_lshl_add_u64 v[72:73], v[146:147], 1, v[72:73]
	v_readlane_b32 s76, v250, 7
	v_readlane_b32 s78, v250, 9
	v_readlane_b32 s79, v250, 10
	v_readlane_b32 s77, v250, 8
	v_readlane_b32 s80, v250, 11
	v_readlane_b32 s81, v250, 12
	v_readlane_b32 s82, v250, 13
	v_readlane_b32 s83, v250, 14
	v_readlane_b32 s84, v250, 15
	v_readlane_b32 s85, v250, 16
	v_readlane_b32 s86, v250, 17
	v_readlane_b32 s87, v250, 18
	v_readlane_b32 s88, v250, 19
	v_readlane_b32 s89, v250, 20
	v_readlane_b32 s90, v250, 21
	v_readlane_b32 s91, v250, 22
	s_waitcnt vmcnt(1)
	v_fma_f32 v60, v76, v64, v60
	s_waitcnt vmcnt(0)
	v_fmac_f32_e32 v59, v76, v71
	v_fma_f32 v61, v76, v65, v61
	v_fma_f32 v62, v76, v66, v62
	v_fmac_f32_e32 v63, v76, v67
	v_fma_f32 v64, v76, v68, v56
	v_fma_f32 v65, v76, v69, v57
	v_fma_f32 v66, v76, v70, v58
	v_cvt_pk_bf16_f32 v56, v60, v61
	v_cvt_pk_bf16_f32 v57, v62, v63
	v_cvt_pk_bf16_f32 v58, v64, v65
	v_cvt_pk_bf16_f32 v59, v66, v59
	global_store_dwordx4 v[72:73], v[56:59], off
	global_load_dwordx4 v[62:65], v[74:75], off offset:512 nt
	global_load_dwordx4 v[66:69], v[74:75], off offset:528 nt
	v_add_u32_e32 v56, 0x90, v148
	v_mul_hi_i32 v57, v56, s43
	v_lshrrev_b32_e32 v58, 31, v57
	v_ashrrev_i32_e32 v57, 10, v57
	v_add_u32_e32 v58, v57, v58
	v_mad_i32_i24 v60, v58, s44, v56
	v_cmp_lt_i32_e32 vcc, s45, v60
	s_waitcnt vmcnt(1)
	v_fma_f32 v52, v76, v62, v52
	v_fma_f32 v53, v76, v63, v53
	v_fma_f32 v54, v76, v64, v54
	v_fmac_f32_e32 v55, v76, v65
	s_waitcnt vmcnt(0)
	v_fma_f32 v57, v76, v66, v48
	v_fma_f32 v59, v76, v67, v49
	v_fmac_f32_e32 v51, v76, v69
	v_cvt_pk_bf16_f32 v48, v52, v53
	v_cvt_pk_bf16_f32 v49, v54, v55
	v_fma_f32 v61, v76, v68, v50
	v_cvt_pk_bf16_f32 v50, v57, v59
	v_cvt_pk_bf16_f32 v51, v61, v51
	global_store_dwordx4 v[72:73], v[48:51], off offset:256
	s_nop 1
	v_mov_b64_e32 v[48:49], s[78:79]
	s_and_saveexec_b64 s[18:19], vcc
	s_xor_b64 s[18:19], exec, s[18:19]
	s_cbranch_execz .LBB0_445
	v_ashrrev_i32_e32 v59, 31, v58
	v_readlane_b32 s76, v250, 7
	v_lshlrev_b64 v[48:49], 25, v[58:59]
	v_readlane_b32 s77, v250, 8
	v_add_u32_e32 v136, 0xffffff80, v60
	v_readlane_b32 s78, v250, 9
	v_lshl_add_u64 v[48:49], s[76:77], 0, v[48:49]
	v_readlane_b32 s79, v250, 10
	v_readlane_b32 s80, v250, 11
	v_readlane_b32 s81, v250, 12
	v_readlane_b32 s82, v250, 13
	v_readlane_b32 s83, v250, 14
	v_readlane_b32 s84, v250, 15
	v_readlane_b32 s85, v250, 16
	v_readlane_b32 s86, v250, 17
	v_readlane_b32 s87, v250, 18
	v_readlane_b32 s88, v250, 19
	v_readlane_b32 s89, v250, 20
	v_readlane_b32 s90, v250, 21
	v_readlane_b32 s91, v250, 22
.LBB0_445:
	s_andn2_saveexec_b64 s[18:19], s[18:19]
	v_max_i32_e32 v50, 0x70, v60
	v_add_u32_e32 v136, 0xffffff90, v50
	s_or_b64 exec, exec, s[18:19]
	v_lshlrev_b64 v[50:51], 13, v[136:137]
	v_lshl_add_u64 v[48:49], v[48:49], 0, v[50:51]
	v_lshl_add_u64 v[58:59], v[146:147], 2, v[48:49]
	global_load_dwordx4 v[48:51], v[58:59], off nt
	global_load_dwordx4 v[52:55], v[58:59], off offset:16 nt
	v_ashrrev_i32_e32 v57, 31, v56
	v_cmp_gt_i32_e32 vcc, s46, v60
	v_lshlrev_b64 v[56:57], 12, v[56:57]
	v_lshl_add_u64 v[56:57], s[96:97], 0, v[56:57]
	v_cndmask_b32_e64 v60, 1.0, 0, vcc
	v_lshl_add_u64 v[56:57], v[146:147], 1, v[56:57]
	v_readlane_b32 s76, v250, 7
	v_readlane_b32 s78, v250, 9
	v_readlane_b32 s79, v250, 10
	v_readlane_b32 s77, v250, 8
	v_readlane_b32 s80, v250, 11
	v_readlane_b32 s81, v250, 12
	v_readlane_b32 s82, v250, 13
	v_readlane_b32 s83, v250, 14
	v_readlane_b32 s84, v250, 15
	v_readlane_b32 s85, v250, 16
	v_readlane_b32 s86, v250, 17
	v_readlane_b32 s87, v250, 18
	v_readlane_b32 s88, v250, 19
	v_readlane_b32 s89, v250, 20
	v_readlane_b32 s90, v250, 21
	v_readlane_b32 s91, v250, 22
	s_waitcnt vmcnt(1)
	v_fma_f32 v44, v60, v48, v44
	s_waitcnt vmcnt(0)
	v_fmac_f32_e32 v43, v60, v55
	v_fma_f32 v45, v60, v49, v45
	v_fma_f32 v46, v60, v50, v46
	v_fmac_f32_e32 v47, v60, v51
	v_fma_f32 v48, v60, v52, v40
	v_fma_f32 v49, v60, v53, v41
	v_fma_f32 v50, v60, v54, v42
	v_cvt_pk_bf16_f32 v40, v44, v45
	v_cvt_pk_bf16_f32 v41, v46, v47
	v_cvt_pk_bf16_f32 v42, v48, v49
	v_cvt_pk_bf16_f32 v43, v50, v43
	global_store_dwordx4 v[56:57], v[40:43], off
	global_load_dwordx4 v[46:49], v[58:59], off offset:512 nt
	global_load_dwordx4 v[50:53], v[58:59], off offset:528 nt
	v_add_u32_e32 v40, 0xa0, v148
	v_mul_hi_i32 v41, v40, s43
	v_lshrrev_b32_e32 v42, 31, v41
	v_ashrrev_i32_e32 v41, 10, v41
	v_add_u32_e32 v42, v41, v42
	v_mad_i32_i24 v44, v42, s44, v40
	v_cmp_lt_i32_e32 vcc, s45, v44
	s_waitcnt vmcnt(1)
	v_fma_f32 v36, v60, v46, v36
	v_fma_f32 v37, v60, v47, v37
	v_fma_f32 v38, v60, v48, v38
	v_fmac_f32_e32 v39, v60, v49
	s_waitcnt vmcnt(0)
	v_fma_f32 v41, v60, v50, v32
	v_fma_f32 v43, v60, v51, v33
	v_fmac_f32_e32 v35, v60, v53
	v_cvt_pk_bf16_f32 v32, v36, v37
	v_cvt_pk_bf16_f32 v33, v38, v39
	v_fma_f32 v45, v60, v52, v34
	v_cvt_pk_bf16_f32 v34, v41, v43
	v_cvt_pk_bf16_f32 v35, v45, v35
	global_store_dwordx4 v[56:57], v[32:35], off offset:256
	s_nop 1
	v_mov_b64_e32 v[32:33], s[78:79]
	s_and_saveexec_b64 s[18:19], vcc
	s_xor_b64 s[18:19], exec, s[18:19]
	s_cbranch_execz .LBB0_449
	v_ashrrev_i32_e32 v43, 31, v42
	v_readlane_b32 s76, v250, 7
	v_lshlrev_b64 v[32:33], 25, v[42:43]
	v_readlane_b32 s77, v250, 8
	v_add_u32_e32 v136, 0xffffff80, v44
	v_readlane_b32 s78, v250, 9
	v_lshl_add_u64 v[32:33], s[76:77], 0, v[32:33]
	v_readlane_b32 s79, v250, 10
	v_readlane_b32 s80, v250, 11
	v_readlane_b32 s81, v250, 12
	v_readlane_b32 s82, v250, 13
	v_readlane_b32 s83, v250, 14
	v_readlane_b32 s84, v250, 15
	v_readlane_b32 s85, v250, 16
	v_readlane_b32 s86, v250, 17
	v_readlane_b32 s87, v250, 18
	v_readlane_b32 s88, v250, 19
	v_readlane_b32 s89, v250, 20
	v_readlane_b32 s90, v250, 21
	v_readlane_b32 s91, v250, 22
.LBB0_449:
	s_andn2_saveexec_b64 s[18:19], s[18:19]
	v_max_i32_e32 v34, 0x70, v44
	v_add_u32_e32 v136, 0xffffff90, v34
	s_or_b64 exec, exec, s[18:19]
	v_lshlrev_b64 v[34:35], 13, v[136:137]
	v_lshl_add_u64 v[32:33], v[32:33], 0, v[34:35]
	v_lshl_add_u64 v[42:43], v[146:147], 2, v[32:33]
	global_load_dwordx4 v[32:35], v[42:43], off nt
	global_load_dwordx4 v[36:39], v[42:43], off offset:16 nt
	v_ashrrev_i32_e32 v41, 31, v40
	v_cmp_gt_i32_e32 vcc, s46, v44
	v_lshlrev_b64 v[40:41], 12, v[40:41]
	v_lshl_add_u64 v[40:41], s[96:97], 0, v[40:41]
	v_cndmask_b32_e64 v44, 1.0, 0, vcc
	v_lshl_add_u64 v[40:41], v[146:147], 1, v[40:41]
	v_readlane_b32 s76, v250, 7
	v_readlane_b32 s78, v250, 9
	v_readlane_b32 s79, v250, 10
	v_readlane_b32 s77, v250, 8
	v_readlane_b32 s80, v250, 11
	v_readlane_b32 s81, v250, 12
	v_readlane_b32 s82, v250, 13
	v_readlane_b32 s83, v250, 14
	v_readlane_b32 s84, v250, 15
	v_readlane_b32 s85, v250, 16
	v_readlane_b32 s86, v250, 17
	v_readlane_b32 s87, v250, 18
	v_readlane_b32 s88, v250, 19
	v_readlane_b32 s89, v250, 20
	v_readlane_b32 s90, v250, 21
	v_readlane_b32 s91, v250, 22
	s_waitcnt vmcnt(1)
	v_fma_f32 v28, v44, v32, v28
	s_waitcnt vmcnt(0)
	v_fmac_f32_e32 v27, v44, v39
	v_fma_f32 v29, v44, v33, v29
	v_fma_f32 v30, v44, v34, v30
	v_fmac_f32_e32 v31, v44, v35
	v_fma_f32 v32, v44, v36, v24
	v_fma_f32 v33, v44, v37, v25
	v_fma_f32 v34, v44, v38, v26
	v_cvt_pk_bf16_f32 v24, v28, v29
	v_cvt_pk_bf16_f32 v25, v30, v31
	v_cvt_pk_bf16_f32 v26, v32, v33
	v_cvt_pk_bf16_f32 v27, v34, v27
	global_store_dwordx4 v[40:41], v[24:27], off
	global_load_dwordx4 v[30:33], v[42:43], off offset:512 nt
	global_load_dwordx4 v[34:37], v[42:43], off offset:528 nt
	v_add_u32_e32 v24, 0xb0, v148
	v_mul_hi_i32 v25, v24, s43
	v_lshrrev_b32_e32 v26, 31, v25
	v_ashrrev_i32_e32 v25, 10, v25
	v_add_u32_e32 v26, v25, v26
	v_mad_i32_i24 v28, v26, s44, v24
	v_cmp_lt_i32_e32 vcc, s45, v28
	s_waitcnt vmcnt(1)
	v_fma_f32 v20, v44, v30, v20
	v_fma_f32 v21, v44, v31, v21
	v_fma_f32 v22, v44, v32, v22
	v_fmac_f32_e32 v23, v44, v33
	s_waitcnt vmcnt(0)
	v_fma_f32 v25, v44, v34, v16
	v_fma_f32 v27, v44, v35, v17
	v_fmac_f32_e32 v19, v44, v37
	v_cvt_pk_bf16_f32 v16, v20, v21
	v_cvt_pk_bf16_f32 v17, v22, v23
	v_fma_f32 v29, v44, v36, v18
	v_cvt_pk_bf16_f32 v18, v25, v27
	v_cvt_pk_bf16_f32 v19, v29, v19
	global_store_dwordx4 v[40:41], v[16:19], off offset:256
	s_nop 1
	v_mov_b64_e32 v[16:17], s[78:79]
	s_and_saveexec_b64 s[18:19], vcc
	s_xor_b64 s[18:19], exec, s[18:19]
	s_cbranch_execz .LBB0_453
	v_ashrrev_i32_e32 v27, 31, v26
	v_readlane_b32 s76, v250, 7
	v_lshlrev_b64 v[16:17], 25, v[26:27]
	v_readlane_b32 s77, v250, 8
	v_add_u32_e32 v136, 0xffffff80, v28
	v_readlane_b32 s78, v250, 9
	v_lshl_add_u64 v[16:17], s[76:77], 0, v[16:17]
	v_readlane_b32 s79, v250, 10
	v_readlane_b32 s80, v250, 11
	v_readlane_b32 s81, v250, 12
	v_readlane_b32 s82, v250, 13
	v_readlane_b32 s83, v250, 14
	v_readlane_b32 s84, v250, 15
	v_readlane_b32 s85, v250, 16
	v_readlane_b32 s86, v250, 17
	v_readlane_b32 s87, v250, 18
	v_readlane_b32 s88, v250, 19
	v_readlane_b32 s89, v250, 20
	v_readlane_b32 s90, v250, 21
	v_readlane_b32 s91, v250, 22
.LBB0_453:
	s_andn2_saveexec_b64 s[18:19], s[18:19]
	v_max_i32_e32 v18, 0x70, v28
	v_add_u32_e32 v136, 0xffffff90, v18
	s_or_b64 exec, exec, s[18:19]
	v_lshlrev_b64 v[18:19], 13, v[136:137]
	v_lshl_add_u64 v[16:17], v[16:17], 0, v[18:19]
	v_lshl_add_u64 v[26:27], v[146:147], 2, v[16:17]
	global_load_dwordx4 v[16:19], v[26:27], off nt
	global_load_dwordx4 v[20:23], v[26:27], off offset:16 nt
	v_ashrrev_i32_e32 v25, 31, v24
	v_cmp_gt_i32_e32 vcc, s46, v28
	v_lshlrev_b64 v[24:25], 12, v[24:25]
	v_lshl_add_u64 v[24:25], s[96:97], 0, v[24:25]
	v_cndmask_b32_e64 v28, 1.0, 0, vcc
	v_lshl_add_u64 v[24:25], v[146:147], 1, v[24:25]
	s_andn2_b64 vcc, exec, s[0:1]
	s_mov_b64 s[0:1], -1
	s_waitcnt vmcnt(1)
	v_fma_f32 v12, v28, v16, v12
	s_waitcnt vmcnt(0)
	v_fmac_f32_e32 v11, v28, v23
	v_fma_f32 v13, v28, v17, v13
	v_fma_f32 v14, v28, v18, v14
	v_fmac_f32_e32 v15, v28, v19
	v_fma_f32 v16, v28, v20, v8
	v_fma_f32 v17, v28, v21, v9
	v_fma_f32 v18, v28, v22, v10
	v_cvt_pk_bf16_f32 v8, v12, v13
	v_cvt_pk_bf16_f32 v9, v14, v15
	v_cvt_pk_bf16_f32 v10, v16, v17
	v_cvt_pk_bf16_f32 v11, v18, v11
	global_store_dwordx4 v[24:25], v[8:11], off
	global_load_dwordx4 v[8:11], v[26:27], off offset:512 nt
	s_nop 0
	global_load_dwordx4 v[12:15], v[26:27], off offset:528 nt
	s_waitcnt vmcnt(1)
	v_fma_f32 v4, v28, v8, v4
	s_waitcnt vmcnt(0)
	v_fmac_f32_e32 v3, v28, v15
	v_fma_f32 v5, v28, v9, v5
	v_fma_f32 v6, v28, v10, v6
	v_fmac_f32_e32 v7, v28, v11
	v_fma_f32 v8, v28, v12, v0
	v_fma_f32 v9, v28, v13, v1
	v_fma_f32 v10, v28, v14, v2
	v_cvt_pk_bf16_f32 v0, v4, v5
	v_cvt_pk_bf16_f32 v1, v6, v7
	v_cvt_pk_bf16_f32 v2, v8, v9
	v_cvt_pk_bf16_f32 v3, v10, v3
	global_store_dwordx4 v[24:25], v[0:3], off offset:256
	s_cbranch_vccnz .LBB0_412
	s_andn2_b64 vcc, exec, s[4:5]
	s_cbranch_vccnz .LBB0_411
	s_barrier
	s_branch .LBB0_411
